# speedup vs baseline: 1.0845x; 1.0845x over previous
.LBB1_6:
	s_or_b64 exec, exec, s[6:7]
	s_ashr_i32 s15, s12, 8
	s_addk_i32 s12, 0xc35
	v_and_b32_e32 v83, 31, v0
	s_load_dwordx2 s[26:27], s[0:1], 0x68
	s_load_dwordx2 s[28:29], s[0:1], 0x30
	s_ashr_i32 s33, s12, 8
	v_lshlrev_b32_e32 v82, 3, v83
	s_movk_i32 s37, 0x110
	s_sub_i32 s34, s33, s15
	v_mad_u32_u24 v144, v155, s37, v82
	s_waitcnt vmcnt(22)
	v_cvt_pk_f16_f32 v85, v4, v5
	v_cvt_pk_f16_f32 v84, v2, v3
	s_add_i32 s4, s34, 3
	ds_write_b64 v144, v[84:85]
	s_waitcnt vmcnt(21)
	v_cvt_pk_f16_f32 v85, v8, v9
	v_cvt_pk_f16_f32 v84, v6, v7
	s_and_b32 s5, s2, 7
	ds_write_b64 v144, v[84:85] offset:4352
	s_waitcnt vmcnt(20)
	v_cvt_pk_f16_f32 v85, v76, v77
	v_cvt_pk_f16_f32 v84, v74, v75
	s_ashr_i32 s35, s4, 2
	ds_write_b64 v144, v[84:85] offset:8704
	s_waitcnt vmcnt(19)
	v_cvt_pk_f16_f32 v85, v80, v81
	v_cvt_pk_f16_f32 v84, v78, v79
	v_bfe_u32 v143, v0, 4, 2
	v_cmp_eq_u32_e64 s[12:13], s5, v1
	s_cmp_lt_i32 s35, 1
	v_lshlrev_b32_e32 v142, 2, v0
	ds_write_b64 v144, v[84:85] offset:13056
	s_waitcnt lgkmcnt(0)
	s_barrier
	s_cbranch_scc1 .LBB1_58
	s_load_dwordx2 s[10:11], s[0:1], 0x60
	s_load_dwordx8 s[16:23], s[0:1], 0x38
	s_load_dwordx4 s[4:7], s[0:1], 0x18
	s_load_dwordx2 s[30:31], s[0:1], 0x28
	s_movk_i32 s0, 0x17f
	v_mov_b32_e32 v85, 0x3f800008
	v_cmp_lt_u32_e32 vcc, s0, v0
	s_movk_i32 s0, 0x13f
	s_addk_i32 s2, 0x7f
	v_cndmask_b32_e32 v82, 0, v85, vcc
	v_cmp_lt_u32_e32 vcc, s0, v0
	s_mul_i32 s0, s3, 0x186a
	s_ashr_i32 s1, s0, 31
	s_lshl_b64 s[0:1], s[0:1], 2
	s_cmpk_lt_u32 s2, 0xff
	s_waitcnt lgkmcnt(0)
	s_cselect_b32 s18, s18, s22
	v_cndmask_b32_e32 v85, 0, v85, vcc
	s_cselect_b32 s2, s19, s23
	s_cselect_b32 s19, s17, s21
	s_cselect_b32 s20, s16, s20
	s_add_u32 s16, s18, s0
	s_waitcnt vmcnt(1)
	v_mul_f32_e32 v86, v85, v151
	s_waitcnt vmcnt(0)
	v_mul_f32_e32 v90, v85, v152
	s_addc_u32 s17, s2, s1
	v_min_u32_e32 v85, 0x69, v0
	v_mov_b32_e32 v87, 0x6000
	v_lshl_or_b32 v85, v85, 2, v87
	s_add_u32 s0, s20, s0
	s_addc_u32 s1, s19, s1
	global_load_dword v115, v85, s[16:17]
	global_load_dword v94, v85, s[0:1]
	v_or_b32_e32 v85, 0x5800, v142
	global_load_dword v95, v85, s[16:17]
	global_load_dword v96, v85, s[0:1]
	v_or_b32_e32 v85, 0x5000, v142
	global_load_dword v97, v85, s[16:17]
	global_load_dword v98, v85, s[0:1]
	v_or_b32_e32 v85, 0x4800, v142
	global_load_dword v99, v85, s[16:17]
	global_load_dword v100, v85, s[0:1]
	v_or_b32_e32 v85, 0x4000, v142
	global_load_dword v101, v85, s[16:17]
	global_load_dword v102, v85, s[0:1]
	v_or_b32_e32 v85, 0x3800, v142
	global_load_dword v103, v85, s[16:17]
	global_load_dword v104, v85, s[0:1]
	v_or_b32_e32 v85, 0x3000, v142
	v_or_b32_e32 v87, 0xa00, v0
	global_load_dword v105, v85, s[16:17]
	global_load_dword v106, v85, s[0:1]
	v_lshlrev_b32_e32 v85, 2, v87
	global_load_dword v107, v85, s[16:17]
	global_load_dword v108, v85, s[0:1]
	v_or_b32_e32 v85, 0x2000, v142
	global_load_dword v109, v85, s[16:17]
	global_load_dword v110, v85, s[0:1]
	global_load_dword v112, v142, s[0:1]
	v_or_b32_e32 v88, 0x600, v0
	v_lshlrev_b32_e32 v85, 2, v88
	global_load_dword v111, v85, s[16:17]
	global_load_dword v114, v85, s[0:1]
	v_or_b32_e32 v85, 0x1000, v142
	global_load_dword v117, v85, s[16:17]
	global_load_dword v116, v85, s[0:1]
	global_load_dword v119, v142, s[16:17] offset:2048
	global_load_dword v118, v142, s[0:1] offset:2048
	global_load_dword v122, v142, s[16:17]
	v_lshlrev_b32_e32 v84, 3, v0
	s_add_u32 s0, s4, 0xc35000
	v_lshlrev_b32_e32 v126, 4, v83
	v_mov_b32_e32 v127, 0
	s_movk_i32 s2, 0x200
	s_addc_u32 s1, s5, 0
	v_lshl_add_u64 v[128:129], s[24:25], 0, v[126:127]
	v_and_b32_e32 v83, 0x78, v84
	v_lshlrev_b32_e32 v126, 2, v142
	v_or_b32_e32 v85, 0x200, v0
	v_lshl_add_u64 v[130:131], s[30:31], 0, v[126:127]
	v_add_u32_e32 v152, 0x15400, v126
	v_lshlrev_b32_e32 v126, 1, v83
	v_lshrrev_b32_e32 v228, 7, v126
	v_and_b32_e32 v229, 0x70, v126
	v_mul_u32_u24_e32 v228, 0x61a800, v228
	v_add_u32_e32 v228, v228, v229
	v_mov_b32_e32 v229, 0
	v_mov_b32_e32 v83, s1
	v_mov_b32_e32 v84, s5
	v_cmp_gt_u32_e32 vcc, s2, v0
	v_lshrrev_b32_e32 v157, 4, v85
	v_bfe_u32 v159, v88, 4, 6
	v_cndmask_b32_e32 v85, v83, v84, vcc
	v_mov_b32_e32 v83, s0
	v_mov_b32_e32 v84, s4
	v_cndmask_b32_e32 v84, v83, v84, vcc
	v_lshl_add_u64 v[136:137], s[0:1], 0, v[228:229]
	v_mul_u32_u24_e32 v83, 0x330, v159
	s_movk_i32 s0, 0x100
	v_bfe_u32 v161, v87, 4, 6
	v_lshrrev_b32_e32 v145, 4, v0
	s_movk_i32 s16, 0x330
	v_add3_u32 v160, v83, v126, s0
	v_mul_u32_u24_e32 v83, 0x330, v161
	s_mul_i32 s0, s14, 0x101
	v_mad_u32_u24 v156, v145, s16, v126
	v_lshl_add_u64 v[132:133], s[4:5], 0, v[228:229]
	v_mad_u32_u24 v158, v157, s16, v126
	v_lshl_add_u64 v[134:135], v[84:85], 0, v[228:229]
	v_lshl_add_u64 v[138:139], s[6:7], 0, v[228:229]
	v_add3_u32 v126, v83, v126, s2
	s_cmp_eq_u32 s3, 0
	v_add_u32_e32 v120, s0, v0
	s_mov_b32 s2, 0x5397829d
	s_cselect_b64 s[16:17], -1, 0
	v_ashrrev_i32_e32 v121, 31, v120
	s_ashr_i32 s1, s0, 31
	v_lshl_add_u64 v[140:141], v[120:121], 2, s[10:11]
	s_lshl_b64 s[0:1], s[0:1], 2
	s_add_u32 s18, s10, s0
	s_movk_i32 s3, 0xff3c
	s_addc_u32 s19, s11, s1
	s_mov_b32 s20, 0xff9e
	v_mul_i32_i24_e32 v123, 0xfffffef2, v146
	v_mul_u32_u24_e32 v125, 0x60, v1
	v_mul_f32_e32 v82, v82, v153
	s_movk_i32 s38, 0xff
	v_lshlrev_b32_e32 v124, 4, v143
	s_mov_b32 s36, 0
	v_or_b32_e32 v150, 64, v155
	v_lshrrev_b32_e32 v151, 2, v0
	v_or_b32_e32 v153, 0x50, v155
	v_or_b32_e32 v154, 0x60, v155
	v_or_b32_e32 v155, 0x70, v155
	v_mov_b32_e32 v83, v82
	v_mov_b32_e32 v84, v82
	v_mov_b32_e32 v85, v82
	v_mov_b32_e32 v87, v86
	v_mov_b32_e32 v88, v86
	v_mov_b32_e32 v89, v86
	v_mov_b32_e32 v91, v90
	v_mov_b32_e32 v92, v90
	v_mov_b32_e32 v93, v90
	v_cmp_lt_u32_e64 s[4:5], 63, v0
	v_sub_u32_e32 v162, v149, v162
	v_sub_u32_e32 v163, v163, v164
	v_add_u32_e32 v164, 0x22b80, v142
	s_waitcnt vmcnt(7)
	v_mul_hi_i32 v113, v112, s2
	v_lshrrev_b32_e32 v120, 31, v113
	v_ashrrev_i32_e32 v113, 6, v113
	v_add_u32_e32 v120, v113, v120
	v_mad_u64_u32 v[112:113], s[0:1], v120, s3, v[112:113]
	v_mul_hi_i32 v113, v112, s2
	v_lshrrev_b32_e32 v121, 31, v113
	v_ashrrev_i32_e32 v113, 5, v113
	v_add_u32_e32 v113, v113, v121
	v_lshlrev_b32_e32 v121, 23, v113
	v_mul_lo_u32 v113, v113, s20
	v_add_lshl_u32 v112, v113, v112, 16
	s_waitcnt vmcnt(0)
	v_or3_b32 v168, v121, v122, v112
	v_mul_hi_i32 v112, v118, s2
	v_lshlrev_b32_e32 v120, 2, v120
	v_lshrrev_b32_e32 v113, 31, v112
	v_ashrrev_i32_e32 v112, 6, v112
	v_add_u32_e32 v167, 0x22780, v120
	v_add_u32_e32 v169, 0x22b80, v120
	v_add_u32_e32 v170, 0x22f80, v120
	v_add_u32_e32 v120, v112, v113
	v_mad_u64_u32 v[112:113], s[0:1], v120, s3, v[118:119]
	v_mul_hi_i32 v113, v112, s2
	v_lshrrev_b32_e32 v118, 31, v113
	v_ashrrev_i32_e32 v113, 5, v113
	v_add_u32_e32 v113, v113, v118
	v_lshlrev_b32_e32 v118, 2, v120
	v_lshlrev_b32_e32 v120, 23, v113
	v_mul_lo_u32 v113, v113, s20
	v_add_lshl_u32 v112, v113, v112, 16
	v_or3_b32 v172, v120, v119, v112
	v_mul_hi_i32 v112, v116, s2
	v_lshrrev_b32_e32 v113, 31, v112
	v_ashrrev_i32_e32 v112, 6, v112
	v_add_u32_e32 v171, 0x22780, v118
	v_add_u32_e32 v173, 0x22b80, v118
	v_add_u32_e32 v174, 0x22f80, v118
	v_add_u32_e32 v118, v112, v113
	v_mad_u64_u32 v[112:113], s[0:1], v118, s3, v[116:117]
	v_mul_hi_i32 v113, v112, s2
	v_lshrrev_b32_e32 v116, 31, v113
	v_ashrrev_i32_e32 v113, 5, v113
	v_add_u32_e32 v113, v113, v116
	v_lshlrev_b32_e32 v116, 2, v118
	v_lshlrev_b32_e32 v118, 23, v113
	v_mul_lo_u32 v113, v113, s20
	v_add_lshl_u32 v112, v113, v112, 16
	v_or3_b32 v176, v118, v117, v112
	v_mul_hi_i32 v112, v114, s2
	v_lshrrev_b32_e32 v113, 31, v112
	v_ashrrev_i32_e32 v112, 6, v112
	v_add_u32_e32 v175, 0x22780, v116
	v_add_u32_e32 v177, 0x22b80, v116
	v_add_u32_e32 v178, 0x22f80, v116
	v_add_u32_e32 v116, v112, v113
	v_mad_u64_u32 v[112:113], s[0:1], v116, s3, v[114:115]
	v_mul_hi_i32 v113, v112, s2
	v_lshrrev_b32_e32 v114, 31, v113
	v_ashrrev_i32_e32 v113, 5, v113
	v_add_u32_e32 v113, v113, v114
	v_lshlrev_b32_e32 v114, 2, v116
	v_lshlrev_b32_e32 v116, 23, v113
	v_mul_lo_u32 v113, v113, s20
	v_add_lshl_u32 v112, v113, v112, 16
	v_or3_b32 v180, v116, v111, v112
	v_mul_hi_i32 v111, v110, s2
	v_lshrrev_b32_e32 v112, 31, v111
	v_ashrrev_i32_e32 v111, 6, v111
	v_add_u32_e32 v112, v111, v112
	v_mad_u64_u32 v[110:111], s[0:1], v112, s3, v[110:111]
	v_mul_hi_i32 v111, v110, s2
	v_lshrrev_b32_e32 v113, 31, v111
	v_ashrrev_i32_e32 v111, 5, v111
	v_add_u32_e32 v111, v111, v113
	v_lshlrev_b32_e32 v113, 23, v111
	v_mul_lo_u32 v111, v111, s20
	v_add_lshl_u32 v110, v111, v110, 16
	v_or3_b32 v184, v113, v109, v110
	v_mul_hi_i32 v109, v108, s2
	v_lshrrev_b32_e32 v110, 31, v109
	v_ashrrev_i32_e32 v109, 6, v109
	v_add_u32_e32 v110, v109, v110
	v_mad_u64_u32 v[108:109], s[0:1], v110, s3, v[108:109]
	v_mul_hi_i32 v109, v108, s2
	v_lshrrev_b32_e32 v111, 31, v109
	v_ashrrev_i32_e32 v109, 5, v109
	v_add_u32_e32 v109, v109, v111
	v_lshlrev_b32_e32 v111, 23, v109
	v_mul_lo_u32 v109, v109, s20
	v_add_lshl_u32 v108, v109, v108, 16
	v_or3_b32 v188, v111, v107, v108
	v_mul_hi_i32 v107, v106, s2
	v_lshrrev_b32_e32 v108, 31, v107
	v_ashrrev_i32_e32 v107, 6, v107
	v_add_u32_e32 v108, v107, v108
	v_mad_u64_u32 v[106:107], s[0:1], v108, s3, v[106:107]
	v_mul_hi_i32 v107, v106, s2
	v_lshrrev_b32_e32 v109, 31, v107
	v_ashrrev_i32_e32 v107, 5, v107
	v_add_u32_e32 v107, v107, v109
	v_lshlrev_b32_e32 v109, 23, v107
	v_mul_lo_u32 v107, v107, s20
	v_add_lshl_u32 v106, v107, v106, 16
	v_or3_b32 v192, v109, v105, v106
	v_mul_hi_i32 v105, v104, s2
	v_lshrrev_b32_e32 v106, 31, v105
	v_ashrrev_i32_e32 v105, 6, v105
	v_add_u32_e32 v106, v105, v106
	v_mad_u64_u32 v[104:105], s[0:1], v106, s3, v[104:105]
	v_mul_hi_i32 v105, v104, s2
	v_lshrrev_b32_e32 v107, 31, v105
	v_ashrrev_i32_e32 v105, 5, v105
	v_add_u32_e32 v105, v105, v107
	v_lshlrev_b32_e32 v107, 23, v105
	v_mul_lo_u32 v105, v105, s20
	v_add_lshl_u32 v104, v105, v104, 16
	v_or3_b32 v196, v107, v103, v104
	v_mul_hi_i32 v103, v102, s2
	v_lshrrev_b32_e32 v104, 31, v103
	v_ashrrev_i32_e32 v103, 6, v103
	v_add_u32_e32 v104, v103, v104
	v_mad_u64_u32 v[102:103], s[0:1], v104, s3, v[102:103]
	v_mul_hi_i32 v103, v102, s2
	v_lshrrev_b32_e32 v105, 31, v103
	v_ashrrev_i32_e32 v103, 5, v103
	v_add_u32_e32 v103, v103, v105
	v_lshlrev_b32_e32 v105, 23, v103
	v_mul_lo_u32 v103, v103, s20
	v_add_lshl_u32 v102, v103, v102, 16
	v_or3_b32 v200, v105, v101, v102
	v_mul_hi_i32 v101, v100, s2
	v_lshrrev_b32_e32 v102, 31, v101
	v_ashrrev_i32_e32 v101, 6, v101
	v_add_u32_e32 v102, v101, v102
	v_mad_u64_u32 v[100:101], s[0:1], v102, s3, v[100:101]
	v_mul_hi_i32 v101, v100, s2
	v_lshrrev_b32_e32 v103, 31, v101
	v_ashrrev_i32_e32 v101, 5, v101
	v_add_u32_e32 v101, v101, v103
	v_lshlrev_b32_e32 v103, 23, v101
	v_mul_lo_u32 v101, v101, s20
	v_add_lshl_u32 v100, v101, v100, 16
	v_or3_b32 v204, v103, v99, v100
	v_mul_hi_i32 v99, v98, s2
	v_lshrrev_b32_e32 v100, 31, v99
	v_ashrrev_i32_e32 v99, 6, v99
	v_add_u32_e32 v100, v99, v100
	v_mad_u64_u32 v[98:99], s[0:1], v100, s3, v[98:99]
	v_mul_hi_i32 v99, v98, s2
	v_lshrrev_b32_e32 v101, 31, v99
	v_ashrrev_i32_e32 v99, 5, v99
	v_add_u32_e32 v99, v99, v101
	v_lshlrev_b32_e32 v101, 23, v99
	v_mul_lo_u32 v99, v99, s20
	v_add_lshl_u32 v98, v99, v98, 16
	v_or3_b32 v208, v101, v97, v98
	v_mul_hi_i32 v97, v96, s2
	v_lshrrev_b32_e32 v98, 31, v97
	v_ashrrev_i32_e32 v97, 6, v97
	v_add_u32_e32 v98, v97, v98
	v_mad_u64_u32 v[96:97], s[10:11], v98, s3, v[96:97]
	v_mul_hi_i32 v97, v96, s2
	v_lshrrev_b32_e32 v99, 31, v97
	v_ashrrev_i32_e32 v97, 5, v97
	v_add_u32_e32 v97, v97, v99
	v_lshlrev_b32_e32 v99, 23, v97
	v_mul_lo_u32 v97, v97, s20
	v_add_lshl_u32 v96, v97, v96, 16
	v_or3_b32 v212, v99, v95, v96
	v_mul_hi_i32 v95, v94, s2
	v_lshrrev_b32_e32 v96, 31, v95
	v_ashrrev_i32_e32 v95, 6, v95
	v_add_u32_e32 v96, v95, v96
	v_mad_u64_u32 v[94:95], s[22:23], v96, s3, v[94:95]
	v_mul_hi_i32 v95, v94, s2
	v_lshrrev_b32_e32 v97, 31, v95
	v_ashrrev_i32_e32 v95, 5, v95
	v_add_u32_e32 v95, v95, v97
	v_lshlrev_b32_e32 v97, 23, v95
	v_mul_lo_u32 v95, v95, s20
	v_add_lshl_u32 v94, v95, v94, 16
	v_or3_b32 v217, v97, v115, v94
	v_lshlrev_b32_e32 v94, 2, v146
	v_lshl_or_b32 v220, v143, 8, v94
	v_mul_u32_u24_e32 v94, 0xcc0, v143
	v_lshlrev_b32_e32 v112, 2, v112
	v_lshlrev_b32_e32 v110, 2, v110
	v_lshlrev_b32_e32 v108, 2, v108
	v_lshlrev_b32_e32 v106, 2, v106
	v_lshlrev_b32_e32 v104, 2, v104
	v_lshlrev_b32_e32 v102, 2, v102
	v_lshlrev_b32_e32 v100, 2, v100
	s_movk_i32 s0, 0x26a
	v_lshlrev_b32_e32 v98, 2, v98
	s_movk_i32 s10, 0x6a
	v_lshlrev_b32_e32 v96, 2, v96
	v_add3_u32 v94, v123, v125, v94
	v_mul_u32_u24_e32 v95, 0x110, v146
	s_mov_b32 s2, 0x8800
	v_add_u32_e32 v165, 0x22f80, v142
	v_add_u32_e32 v166, 0x22780, v142
	v_cmp_eq_u32_e64 s[6:7], s38, v0
	v_add_u32_e32 v179, 0x22780, v114
	v_add_u32_e32 v181, 0x22b80, v114
	v_add_u32_e32 v182, 0x22f80, v114
	v_add_u32_e32 v183, 0x22780, v112
	v_add_u32_e32 v185, 0x22b80, v112
	v_add_u32_e32 v186, 0x22f80, v112
	v_add_u32_e32 v187, 0x22780, v110
	v_add_u32_e32 v189, 0x22b80, v110
	v_add_u32_e32 v190, 0x22f80, v110
	v_add_u32_e32 v191, 0x22780, v108
	v_add_u32_e32 v193, 0x22b80, v108
	v_add_u32_e32 v194, 0x22f80, v108
	v_add_u32_e32 v195, 0x22780, v106
	v_add_u32_e32 v197, 0x22b80, v106
	v_add_u32_e32 v198, 0x22f80, v106
	v_add_u32_e32 v199, 0x22780, v104
	v_add_u32_e32 v201, 0x22b80, v104
	v_add_u32_e32 v202, 0x22f80, v104
	v_add_u32_e32 v203, 0x22780, v102
	v_add_u32_e32 v205, 0x22b80, v102
	v_add_u32_e32 v206, 0x22f80, v102
	v_add_u32_e32 v207, 0x22780, v100
	v_add_u32_e32 v209, 0x22b80, v100
	v_add_u32_e32 v210, 0x22f80, v100
	v_cmp_gt_u32_e64 s[0:1], s0, v0
	v_add_u32_e32 v211, 0x22780, v98
	v_add_u32_e32 v213, 0x22b80, v98
	v_add_u32_e32 v214, 0x22f80, v98
	v_cmp_gt_u32_e64 s[10:11], s10, v0
	v_add_u32_e32 v216, 0x22780, v96
	v_add_u32_e32 v218, 0x22b80, v96
	v_add_u32_e32 v219, 0x22f80, v96
	v_add3_u32 v221, v94, v95, s2
	v_mad_u32_u24 v222, v146, s37, v124
	v_mov_b32_e32 v215, 0xff800000
	s_mov_b64 s[20:21], 0
	s_movk_i32 s37, 0x4400
	v_mov_b32_e32 v223, 1

.LBB1_29:
	ds_read_b128 v[94:97], v126 offset:34816
	v_add_u32_e32 v98, s39, v161
	v_ashrrev_i32_e32 v99, 31, v98
	v_lshlrev_b64 v[98:99], 7, v[98:99]
	v_lshl_add_u64 v[98:99], v[138:139], 0, v[98:99]
	s_waitcnt lgkmcnt(0)
	global_store_dwordx4 v[98:99], v[94:97], off

.LBB1_37:
	ds_read_b128 v[94:97], v156 offset:34816
	v_add_u32_e32 v98, s39, v145
	v_ashrrev_i32_e32 v99, 31, v98
	v_lshlrev_b64 v[98:99], 7, v[98:99]
	v_lshl_add_u64 v[98:99], v[132:133], 0, v[98:99]
	s_waitcnt lgkmcnt(0)
	global_store_dwordx4 v[98:99], v[94:97], off
	s_or_b64 exec, exec, s[2:3]
	v_cmp_gt_i32_e64 s[2:3], s25, v157
	s_and_saveexec_b64 s[30:31], s[2:3]
	s_cbranch_execz .LBB1_25
.LBB1_38:
	ds_read_b128 v[94:97], v158 offset:34816
	v_add_u32_e32 v98, s39, v157
	v_ashrrev_i32_e32 v99, 31, v98
	v_lshlrev_b64 v[98:99], 7, v[98:99]
	v_lshl_add_u64 v[98:99], v[134:135], 0, v[98:99]
	s_waitcnt lgkmcnt(0)
	global_store_dwordx4 v[98:99], v[94:97], off
	s_or_b64 exec, exec, s[30:31]
	s_and_saveexec_b64 s[2:3], vcc
	s_cbranch_execz .LBB1_26
.LBB1_39:
	ds_read_b128 v[94:97], v156 offset:35072
	v_add_u32_e32 v98, s39, v145
	v_ashrrev_i32_e32 v99, 31, v98
	v_lshlrev_b64 v[98:99], 7, v[98:99]
	v_lshl_add_u64 v[98:99], v[136:137], 0, v[98:99]
	s_waitcnt lgkmcnt(0)
	global_store_dwordx4 v[98:99], v[94:97], off
	s_or_b64 exec, exec, s[2:3]
	v_cmp_gt_i32_e64 s[2:3], s25, v159
	s_and_saveexec_b64 s[30:31], s[2:3]
	s_cbranch_execz .LBB1_27
.LBB1_40:
	ds_read_b128 v[94:97], v160 offset:34816
	v_add_u32_e32 v98, s39, v159
	v_ashrrev_i32_e32 v99, 31, v98
	v_lshlrev_b64 v[98:99], 7, v[98:99]
	v_lshl_add_u64 v[98:99], v[136:137], 0, v[98:99]
	s_waitcnt lgkmcnt(0)
	global_store_dwordx4 v[98:99], v[94:97], off
	s_or_b64 exec, exec, s[30:31]
	s_and_saveexec_b64 s[2:3], vcc
	s_cbranch_execz .LBB1_28
.LBB1_41:
	ds_read_b128 v[94:97], v156 offset:35328
	v_add_u32_e32 v98, s39, v145
	v_ashrrev_i32_e32 v99, 31, v98
	v_lshlrev_b64 v[98:99], 7, v[98:99]
	v_lshl_add_u64 v[98:99], v[138:139], 0, v[98:99]
	s_waitcnt lgkmcnt(0)
	global_store_dwordx4 v[98:99], v[94:97], off
	s_or_b64 exec, exec, s[2:3]
	v_cmp_gt_i32_e32 vcc, s25, v161
	s_and_saveexec_b64 s[2:3], vcc
	s_cbranch_execnz .LBB1_29
	s_branch .LBB1_30

	.amdhsa_kernel _Z19gemm_scatter_kernelPKfPKDF16_S0_PDF16_S3_PfPjPKiS7_S7_S7_S7_PiS5_
		.amdhsa_group_segment_fixed_size 144320
		.amdhsa_private_segment_fixed_size 0
		.amdhsa_kernarg_size 112
		.amdhsa_user_sgpr_count 2
		.amdhsa_user_sgpr_dispatch_ptr 0
		.amdhsa_user_sgpr_queue_ptr 0
		.amdhsa_user_sgpr_kernarg_segment_ptr 1
		.amdhsa_user_sgpr_dispatch_id 0
		.amdhsa_user_sgpr_kernarg_preload_length 0
		.amdhsa_user_sgpr_kernarg_preload_offset 0
		.amdhsa_user_sgpr_private_segment_size 0
		.amdhsa_uses_dynamic_stack 0
		.amdhsa_enable_private_segment 0
		.amdhsa_system_sgpr_workgroup_id_x 1
		.amdhsa_system_sgpr_workgroup_id_y 0
		.amdhsa_system_sgpr_workgroup_id_z 0
		.amdhsa_system_sgpr_workgroup_info 0
		.amdhsa_system_vgpr_workitem_id 0
		.amdhsa_next_free_vgpr 230
		.amdhsa_next_free_sgpr 96
		.amdhsa_accum_offset 232
		.amdhsa_reserve_vcc 1
		.amdhsa_float_round_mode_32 0
		.amdhsa_float_round_mode_16_64 0
		.amdhsa_float_denorm_mode_32 3
		.amdhsa_float_denorm_mode_16_64 3
		.amdhsa_dx10_clamp 1
		.amdhsa_ieee_mode 1
		.amdhsa_fp16_overflow 0
		.amdhsa_tg_split 0
		.amdhsa_exception_fp_ieee_invalid_op 0
		.amdhsa_exception_fp_denorm_src 0
		.amdhsa_exception_fp_ieee_div_zero 0
		.amdhsa_exception_fp_ieee_overflow 0
		.amdhsa_exception_fp_ieee_underflow 0
		.amdhsa_exception_fp_ieee_inexact 0
		.amdhsa_exception_int_div_zero 0
	.end_amdhsa_kernel

_Z10agg_kernelPKjPKiPKDF16_S4_PKfS4_S0_S2_S2_S2_S2_Pf:
	s_and_b32 s3, s2, 1
	s_lshr_b32 s4, s2, 1
	s_load_dwordx16 s[8:23], s[0:1], 0x0
	s_load_dwordx8 s[24:31], s[0:1], 0x40
	s_mul_i32 s6, s4, 0xc4
	s_sub_u32 s5, 0xc350, s6
	s_min_u32 s5, s5, 0xc4
	v_lshrrev_b32_e32 v2, 2, v0
	v_and_b32_e32 v1, 3, v0
	v_lshrrev_b32_e32 v13, 1, v1
	v_lshl_add_u32 v13, s3, 1, v13
	v_lshlrev_b32_e32 v13, 2, v13
	v_lshlrev_b32_e32 v1, 5, v1
	s_lshl_b32 s52, s4, 2
	s_waitcnt lgkmcnt(0)
	s_add_u32 s52, s10, s52
	s_addc_u32 s53, s11, 0
	s_load_dwordx2 s[32:33], s[52:53], 0x0
	s_load_dwordx2 s[36:37], s[52:53], 0x404
	v_add_u32_e32 v40, s6, v2
	v_min_u32_e32 v40, 0xc34f, v40
	v_lshlrev_b32_e32 v40, 6, v40
	v_add3_u32 v40, v40, v13, 16
	global_load_dword v3, v40, s[16:17]
	global_load_dword v4, v40, s[16:17] offset:32
	v_lshlrev_b32_e32 v62, 2, v0
	v_mov_b32_e32 v63, 0
	ds_write_b32 v62, v63 offset:32768
	s_waitcnt lgkmcnt(0)
	s_sub_u32 s38, s33, s32
	s_sub_u32 s39, s37, s36
	s_lshl_b32 s52, s32, 2
	s_add_u32 s42, s8, s52
	s_addc_u32 s43, s9, 0
	s_add_u32 s52, s36, 0xc3500
	s_lshl_b32 s52, s52, 2
	s_add_u32 s44, s8, s52
	s_addc_u32 s45, s9, 0
	s_max_i32 s52, s38, 1
	s_sub_u32 s52, s52, 1
	s_max_i32 s53, s39, 1
	s_sub_u32 s53, s53, 1
	s_movk_i32 s46, 0x80
	s_movk_i32 s55, 0x62
	s_movk_i32 s47, 0x61a8
	v_min_u32_e32 v41, s52, v0
	v_lshlrev_b32_e32 v41, 2, v41
	global_load_dword v8, v41, s[42:43]
	v_min_u32_e32 v41, s53, v0
	v_lshlrev_b32_e32 v41, 2, v41
	global_load_dword v24, v41, s[44:45]
	v_add_u32_e32 v40, 0x400, v0
	v_min_u32_e32 v41, s52, v40
	v_lshlrev_b32_e32 v41, 2, v41
	global_load_dword v9, v41, s[42:43]
	v_min_u32_e32 v41, s53, v40
	v_lshlrev_b32_e32 v41, 2, v41
	global_load_dword v25, v41, s[44:45]
	v_add_u32_e32 v40, 0x800, v0
	v_min_u32_e32 v41, s52, v40
	v_lshlrev_b32_e32 v41, 2, v41
	global_load_dword v10, v41, s[42:43]
	v_min_u32_e32 v41, s53, v40
	v_lshlrev_b32_e32 v41, 2, v41
	global_load_dword v26, v41, s[44:45]
	v_add_u32_e32 v40, 0xc00, v0
	v_min_u32_e32 v41, s52, v40
	v_lshlrev_b32_e32 v41, 2, v41
	global_load_dword v11, v41, s[42:43]
	v_min_u32_e32 v41, s53, v40
	v_lshlrev_b32_e32 v41, 2, v41
	global_load_dword v27, v41, s[44:45]
	v_mov_b32_e32 v61, 1
	v_mov_b32_e32 v43, 0xc4
	s_barrier
	s_waitcnt vmcnt(7)
	v_bfe_u32 v41, v8, 16, 7
	v_bfe_u32 v42, v8, 23, 1
	v_and_b32_e32 v44, 0xffff, v8
	v_mad_u32_u24 v41, v42, s55, v41
	v_cmp_le_u32_e32 vcc, s47, v44
	v_lshlrev_b32_e32 v41, 2, v41
	s_nop 0
	v_cndmask_b32_e32 v42, 0, v43, vcc
	v_lshl_add_u32 v41, v42, 2, v41
	v_cmp_gt_u32_e32 vcc, s38, v0
	s_and_saveexec_b64 s[60:61], vcc
	ds_add_rtn_u32 v16, v41, v61 offset:32768
	s_mov_b64 exec, s[60:61]
	s_waitcnt vmcnt(6)
	v_bfe_u32 v41, v24, 16, 7
	v_bfe_u32 v42, v24, 23, 1
	v_and_b32_e32 v44, 0xffff, v24
	v_mad_u32_u24 v41, v42, s55, v41
	v_cmp_le_u32_e32 vcc, s47, v44
	v_lshlrev_b32_e32 v41, 2, v41
	s_nop 0
	v_cndmask_b32_e32 v42, 0, v43, vcc
	v_lshl_add_u32 v41, v42, 2, v41
	v_cmp_gt_u32_e32 vcc, s39, v0
	s_and_saveexec_b64 s[60:61], vcc
	ds_add_rtn_u32 v20, v41, v61 offset:34816
	s_mov_b64 exec, s[60:61]
	s_waitcnt vmcnt(5)
	v_add_u32_e32 v40, 0x400, v0
	v_bfe_u32 v41, v9, 16, 7
	v_bfe_u32 v42, v9, 23, 1
	v_and_b32_e32 v44, 0xffff, v9
	v_mad_u32_u24 v41, v42, s55, v41
	v_cmp_le_u32_e32 vcc, s47, v44
	v_lshlrev_b32_e32 v41, 2, v41
	s_nop 0
	v_cndmask_b32_e32 v42, 0, v43, vcc
	v_lshl_add_u32 v41, v42, 2, v41
	v_cmp_gt_u32_e32 vcc, s38, v40
	s_and_saveexec_b64 s[60:61], vcc
	ds_add_rtn_u32 v17, v41, v61 offset:32768
	s_mov_b64 exec, s[60:61]
	s_waitcnt vmcnt(4)
	v_bfe_u32 v41, v25, 16, 7
	v_bfe_u32 v42, v25, 23, 1
	v_and_b32_e32 v44, 0xffff, v25
	v_mad_u32_u24 v41, v42, s55, v41
	v_cmp_le_u32_e32 vcc, s47, v44
	v_lshlrev_b32_e32 v41, 2, v41
	s_nop 0
	v_cndmask_b32_e32 v42, 0, v43, vcc
	v_lshl_add_u32 v41, v42, 2, v41
	v_cmp_gt_u32_e32 vcc, s39, v40
	s_and_saveexec_b64 s[60:61], vcc
	ds_add_rtn_u32 v21, v41, v61 offset:34816
	s_mov_b64 exec, s[60:61]
	s_waitcnt vmcnt(3)
	v_add_u32_e32 v40, 0x800, v0
	v_bfe_u32 v41, v10, 16, 7
	v_bfe_u32 v42, v10, 23, 1
	v_and_b32_e32 v44, 0xffff, v10
	v_mad_u32_u24 v41, v42, s55, v41
	v_cmp_le_u32_e32 vcc, s47, v44
	v_lshlrev_b32_e32 v41, 2, v41
	s_nop 0
	v_cndmask_b32_e32 v42, 0, v43, vcc
	v_lshl_add_u32 v41, v42, 2, v41
	v_cmp_gt_u32_e32 vcc, s38, v40
	s_and_saveexec_b64 s[60:61], vcc
	ds_add_rtn_u32 v18, v41, v61 offset:32768
	s_mov_b64 exec, s[60:61]
	s_waitcnt vmcnt(2)
	v_bfe_u32 v41, v26, 16, 7
	v_bfe_u32 v42, v26, 23, 1
	v_and_b32_e32 v44, 0xffff, v26
	v_mad_u32_u24 v41, v42, s55, v41
	v_cmp_le_u32_e32 vcc, s47, v44
	v_lshlrev_b32_e32 v41, 2, v41
	s_nop 0
	v_cndmask_b32_e32 v42, 0, v43, vcc
	v_lshl_add_u32 v41, v42, 2, v41
	v_cmp_gt_u32_e32 vcc, s39, v40
	s_and_saveexec_b64 s[60:61], vcc
	ds_add_rtn_u32 v22, v41, v61 offset:34816
	s_mov_b64 exec, s[60:61]
	s_waitcnt vmcnt(1)
	v_add_u32_e32 v40, 0xc00, v0
	v_bfe_u32 v41, v11, 16, 7
	v_bfe_u32 v42, v11, 23, 1
	v_and_b32_e32 v44, 0xffff, v11
	v_mad_u32_u24 v41, v42, s55, v41
	v_cmp_le_u32_e32 vcc, s47, v44
	v_lshlrev_b32_e32 v41, 2, v41
	s_nop 0
	v_cndmask_b32_e32 v42, 0, v43, vcc
	v_lshl_add_u32 v41, v42, 2, v41
	v_cmp_gt_u32_e32 vcc, s38, v40
	s_and_saveexec_b64 s[60:61], vcc
	ds_add_rtn_u32 v19, v41, v61 offset:32768
	s_mov_b64 exec, s[60:61]
	s_waitcnt vmcnt(0)
	v_bfe_u32 v41, v27, 16, 7
	v_bfe_u32 v42, v27, 23, 1
	v_and_b32_e32 v44, 0xffff, v27
	v_mad_u32_u24 v41, v42, s55, v41
	v_cmp_le_u32_e32 vcc, s47, v44
	v_lshlrev_b32_e32 v41, 2, v41
	s_nop 0
	v_cndmask_b32_e32 v42, 0, v43, vcc
	v_lshl_add_u32 v41, v42, 2, v41
	v_cmp_gt_u32_e32 vcc, s39, v40
	s_and_saveexec_b64 s[60:61], vcc
	ds_add_rtn_u32 v23, v41, v61 offset:34816
	s_mov_b64 exec, s[60:61]
	s_waitcnt lgkmcnt(0)
	s_barrier
	ds_read_b32 v40, v62 offset:32768
	v_and_b32_e32 v44, 63, v0
	v_lshrrev_b32_e32 v45, 6, v0
	v_lshlrev_b32_e32 v45, 2, v45
	s_waitcnt lgkmcnt(0)
	v_mov_b32_e32 v41, v40
	s_nop 1
	v_add_u32_dpp v41, v41, v41 row_shr:1 row_mask:0xf bank_mask:0xf
	s_nop 1
	v_add_u32_dpp v41, v41, v41 row_shr:2 row_mask:0xf bank_mask:0xf
	s_nop 1
	v_add_u32_dpp v41, v41, v41 row_shr:4 row_mask:0xf bank_mask:0xf
	s_nop 1
	v_add_u32_dpp v41, v41, v41 row_shr:8 row_mask:0xf bank_mask:0xf
	s_nop 1
	v_add_u32_dpp v41, v41, v41 row_bcast:15 row_mask:0xa bank_mask:0xf
	s_nop 1
	v_add_u32_dpp v41, v41, v41 row_bcast:31 row_mask:0xc bank_mask:0xf
	v_cmp_eq_u32_e32 vcc, 63, v44
	s_and_saveexec_b64 s[60:61], vcc
	ds_write_b32 v45, v41 offset:40960
	s_mov_b64 exec, s[60:61]
	s_waitcnt lgkmcnt(0)
	s_barrier
	v_cmp_gt_u32_e32 vcc, 64, v0
	s_and_saveexec_b64 s[60:61], vcc
	s_cbranch_execz .Lagg_w0_done
	v_and_b32_e32 v46, 7, v0
	v_lshrrev_b32_e32 v47, 4, v0
	v_lshl_add_u32 v46, v47, 3, v46
	v_lshlrev_b32_e32 v46, 2, v46
	v_and_b32_e32 v47, 0x28, v0
	v_mov_b32_e32 v48, 0
	v_cmp_eq_u32_e32 vcc, 0, v47
	s_and_saveexec_b64 s[62:63], vcc
	ds_read_b32 v48, v46 offset:40960
	s_waitcnt lgkmcnt(0)
	s_mov_b64 exec, s[62:63]
	v_mov_b32_e32 v49, v48
	s_nop 1
	v_add_u32_dpp v49, v49, v49 row_shr:1 row_mask:0xf bank_mask:0xf
	s_nop 1
	v_add_u32_dpp v49, v49, v49 row_shr:2 row_mask:0xf bank_mask:0xf
	s_nop 1
	v_add_u32_dpp v49, v49, v49 row_shr:4 row_mask:0xf bank_mask:0xf
	s_nop 1
	v_sub_u32_e32 v50, v49, v48
	s_and_b64 exec, exec, vcc
	ds_write_b32 v46, v50 offset:41024
	ds_write_b32 v46, v49 offset:41088
.Lagg_w0_done:
	s_mov_b64 exec, s[60:61]
	s_waitcnt lgkmcnt(0)
	s_barrier
	ds_read_b32 v46, v45 offset:41024
	v_mov_b32_e32 v47, 0
	ds_read_b32 v48, v47 offset:41116
	ds_read_b32 v49, v47 offset:41148
	v_sub_u32_e32 v41, v41, v40
	s_waitcnt lgkmcnt(0)
	v_add_u32_e32 v41, v41, v46
	ds_write_b32 v62, v41 offset:36864
	v_max_u32_e32 v48, v48, v49
	s_nop 0
	v_readfirstlane_b32 s52, v48
	s_cmpk_le_u32 s52, 0x2000
	s_cselect_b32 s7, 1, 0
	s_max_u32 s52, s38, s39
	s_cmpk_le_u32 s52, 0x1000
	s_cselect_b32 s7, s7, 0
	s_waitcnt lgkmcnt(0)
	s_barrier
	s_cmp_eq_u32 s7, 0
	s_cbranch_scc1 .Lagg_scatter_done
	v_bfe_u32 v48, v8, 16, 7
	v_bfe_u32 v42, v8, 23, 1
	v_and_b32_e32 v44, 0xffff, v8
	v_mad_u32_u24 v48, v42, s55, v48
	v_cmp_le_u32_e32 vcc, s47, v44
	v_lshlrev_b32_e32 v48, 2, v48
	s_nop 0
	v_cndmask_b32_e32 v42, 0, v43, vcc
	v_lshl_add_u32 v48, v42, 2, v48
	ds_read_b32 v48, v48 offset:36864
	v_bfe_u32 v49, v9, 16, 7
	v_bfe_u32 v42, v9, 23, 1
	v_and_b32_e32 v44, 0xffff, v9
	v_mad_u32_u24 v49, v42, s55, v49
	v_cmp_le_u32_e32 vcc, s47, v44
	v_lshlrev_b32_e32 v49, 2, v49
	s_nop 0
	v_cndmask_b32_e32 v42, 0, v43, vcc
	v_lshl_add_u32 v49, v42, 2, v49
	ds_read_b32 v49, v49 offset:36864
	v_bfe_u32 v50, v10, 16, 7
	v_bfe_u32 v42, v10, 23, 1
	v_and_b32_e32 v44, 0xffff, v10
	v_mad_u32_u24 v50, v42, s55, v50
	v_cmp_le_u32_e32 vcc, s47, v44
	v_lshlrev_b32_e32 v50, 2, v50
	s_nop 0
	v_cndmask_b32_e32 v42, 0, v43, vcc
	v_lshl_add_u32 v50, v42, 2, v50
	ds_read_b32 v50, v50 offset:36864
	v_bfe_u32 v51, v11, 16, 7
	v_bfe_u32 v42, v11, 23, 1
	v_and_b32_e32 v44, 0xffff, v11
	v_mad_u32_u24 v51, v42, s55, v51
	v_cmp_le_u32_e32 vcc, s47, v44
	v_lshlrev_b32_e32 v51, 2, v51
	s_nop 0
	v_cndmask_b32_e32 v42, 0, v43, vcc
	v_lshl_add_u32 v51, v42, 2, v51
	ds_read_b32 v51, v51 offset:36864
	s_waitcnt lgkmcnt(3)
	v_add_u32_e32 v48, v48, v16
	v_lshlrev_b32_e32 v48, 1, v48
	s_waitcnt lgkmcnt(2)
	v_add_u32_e32 v49, v49, v17
	v_lshlrev_b32_e32 v49, 1, v49
	s_waitcnt lgkmcnt(1)
	v_add_u32_e32 v50, v50, v18
	v_lshlrev_b32_e32 v50, 1, v50
	s_waitcnt lgkmcnt(0)
	v_add_u32_e32 v51, v51, v19
	v_lshlrev_b32_e32 v51, 1, v51
	v_cmp_gt_u32_e32 vcc, s38, v0
	s_and_saveexec_b64 s[60:61], vcc
	ds_write_b16 v48, v8 offset:0
	s_mov_b64 exec, s[60:61]
	v_add_u32_e32 v40, 0x400, v0
	v_cmp_gt_u32_e32 vcc, s38, v40
	s_and_saveexec_b64 s[60:61], vcc
	ds_write_b16 v49, v9 offset:0
	s_mov_b64 exec, s[60:61]
	v_add_u32_e32 v40, 0x800, v0
	v_cmp_gt_u32_e32 vcc, s38, v40
	s_and_saveexec_b64 s[60:61], vcc
	ds_write_b16 v50, v10 offset:0
	s_mov_b64 exec, s[60:61]
	v_add_u32_e32 v40, 0xc00, v0
	v_cmp_gt_u32_e32 vcc, s38, v40
	s_and_saveexec_b64 s[60:61], vcc
	ds_write_b16 v51, v11 offset:0
	s_mov_b64 exec, s[60:61]
	v_bfe_u32 v48, v24, 16, 7
	v_bfe_u32 v42, v24, 23, 1
	v_and_b32_e32 v44, 0xffff, v24
	v_mad_u32_u24 v48, v42, s55, v48
	v_cmp_le_u32_e32 vcc, s47, v44
	v_lshlrev_b32_e32 v48, 2, v48
	s_nop 0
	v_cndmask_b32_e32 v42, 0, v43, vcc
	v_lshl_add_u32 v48, v42, 2, v48
	ds_read_b32 v48, v48 offset:38912
	v_bfe_u32 v49, v25, 16, 7
	v_bfe_u32 v42, v25, 23, 1
	v_and_b32_e32 v44, 0xffff, v25
	v_mad_u32_u24 v49, v42, s55, v49
	v_cmp_le_u32_e32 vcc, s47, v44
	v_lshlrev_b32_e32 v49, 2, v49
	s_nop 0
	v_cndmask_b32_e32 v42, 0, v43, vcc
	v_lshl_add_u32 v49, v42, 2, v49
	ds_read_b32 v49, v49 offset:38912
	v_bfe_u32 v50, v26, 16, 7
	v_bfe_u32 v42, v26, 23, 1
	v_and_b32_e32 v44, 0xffff, v26
	v_mad_u32_u24 v50, v42, s55, v50
	v_cmp_le_u32_e32 vcc, s47, v44
	v_lshlrev_b32_e32 v50, 2, v50
	s_nop 0
	v_cndmask_b32_e32 v42, 0, v43, vcc
	v_lshl_add_u32 v50, v42, 2, v50
	ds_read_b32 v50, v50 offset:38912
	v_bfe_u32 v51, v27, 16, 7
	v_bfe_u32 v42, v27, 23, 1
	v_and_b32_e32 v44, 0xffff, v27
	v_mad_u32_u24 v51, v42, s55, v51
	v_cmp_le_u32_e32 vcc, s47, v44
	v_lshlrev_b32_e32 v51, 2, v51
	s_nop 0
	v_cndmask_b32_e32 v42, 0, v43, vcc
	v_lshl_add_u32 v51, v42, 2, v51
	ds_read_b32 v51, v51 offset:38912
	s_waitcnt lgkmcnt(3)
	v_add_u32_e32 v48, v48, v20
	v_lshlrev_b32_e32 v48, 1, v48
	s_waitcnt lgkmcnt(2)
	v_add_u32_e32 v49, v49, v21
	v_lshlrev_b32_e32 v49, 1, v49
	s_waitcnt lgkmcnt(1)
	v_add_u32_e32 v50, v50, v22
	v_lshlrev_b32_e32 v50, 1, v50
	s_waitcnt lgkmcnt(0)
	v_add_u32_e32 v51, v51, v23
	v_lshlrev_b32_e32 v51, 1, v51
	v_cmp_gt_u32_e32 vcc, s39, v0
	s_and_saveexec_b64 s[60:61], vcc
	ds_write_b16 v48, v24 offset:16384
	s_mov_b64 exec, s[60:61]
	v_add_u32_e32 v40, 0x400, v0
	v_cmp_gt_u32_e32 vcc, s39, v40
	s_and_saveexec_b64 s[60:61], vcc
	ds_write_b16 v49, v25 offset:16384
	s_mov_b64 exec, s[60:61]
	v_add_u32_e32 v40, 0x800, v0
	v_cmp_gt_u32_e32 vcc, s39, v40
	s_and_saveexec_b64 s[60:61], vcc
	ds_write_b16 v50, v26 offset:16384
	s_mov_b64 exec, s[60:61]
	v_add_u32_e32 v40, 0xc00, v0
	v_cmp_gt_u32_e32 vcc, s39, v40
	s_and_saveexec_b64 s[60:61], vcc
	ds_write_b16 v51, v27 offset:16384
	s_mov_b64 exec, s[60:61]
.Lagg_scatter_done:
	s_waitcnt vmcnt(0) lgkmcnt(0)
	s_barrier
	v_mov_b32_e32 v24, 0
	v_mov_b32_e32 v25, 0
	v_mov_b32_e32 v26, 0
	v_mov_b32_e32 v27, 0
	v_mov_b32_e32 v28, 0
	v_mov_b32_e32 v29, 0
	v_mov_b32_e32 v30, 0
	v_mov_b32_e32 v31, 0
	v_mov_b32_e32 v32, 0
	v_mov_b32_e32 v33, 0
	v_mov_b32_e32 v34, 0
	v_mov_b32_e32 v35, 0
	v_mov_b32_e32 v36, 0
	v_mov_b32_e32 v37, 0
	v_mov_b32_e32 v38, 0
	v_mov_b32_e32 v39, 0
	v_mov_b32_e32 v15, 1.0
	s_lshl_b32 s52, s3, 8
	s_add_u32 s68, s30, s52
	s_addc_u32 s69, s31, 0
	s_mul_i32 s52, s3, 0x61a800
	s_add_u32 s70, s14, s52
	s_addc_u32 s71, s15, 0
	v_cmp_gt_u32_e32 vcc, s5, v2
	s_and_saveexec_b64 s[56:57], vcc
	s_cbranch_execz .Lagg_exit
	s_mul_i32 s52, s3, 0x61a800
	s_add_u32 s48, s12, s52
	s_addc_u32 s49, s13, 0
	s_lshl_b32 s52, s3, 7
	s_add_u32 s52, s18, s52
	s_addc_u32 s53, s19, 0
	global_load_dwordx4 v[16:19], v1, s[52:53]
	global_load_dwordx4 v[20:23], v1, s[52:53] offset:16
	global_load_dword v56, v13, s[20:21] offset:0
	global_load_dword v57, v13, s[20:21] offset:16
	s_waitcnt vmcnt(0)
	v_not_b32_e32 v58, v56
	v_and_b32_e32 v59, 0x7fffffff, v56
	v_cmp_gt_i32_e32 vcc, 0, v56
	s_nop 1
	v_cndmask_b32_e32 v56, v58, v59, vcc
	v_not_b32_e32 v58, v57
	v_and_b32_e32 v59, 0x7fffffff, v57
	v_cmp_gt_i32_e32 vcc, 0, v57
	s_nop 1
	v_cndmask_b32_e32 v57, v58, v59, vcc
	v_add_f32_e32 v14, v56, v57
	v_mul_f32_e32 v58, 0x3c23d70a, v14
	v_max_f32_e32 v14, v14, v58
	v_add_f32_e32 v46, v56, v3
	v_mul_f32_e32 v58, 0x3c23d70a, v46
	v_max_f32_e32 v46, v46, v58
	v_sub_f32_e32 v43, v3, v46
	v_mul_f32_e32 v43, 0.5, v43
	v_mul_f32_e32 v44, 0xbf7d70a4, v46
	v_mov_b32_e32 v45, 0
	v_mov_b32_e32 v48, 0
	v_mov_b32_e32 v49, 0
	v_mov_b32_e32 v50, 0
	v_mov_b32_e32 v51, 0
	v_mov_b32_e32 v52, 0
	v_mov_b32_e32 v53, 0
	v_mov_b32_e32 v54, 0
	v_mov_b32_e32 v55, 0
	s_cmp_eq_u32 s7, 0
	s_cbranch_scc1 .Lagg_slow_0
	v_lshlrev_b32_e32 v61, 2, v2
	ds_read_b32 v59, v61 offset:32768
	ds_read_b32 v60, v61 offset:36864
	s_waitcnt lgkmcnt(0)
	v_lshlrev_b32_e32 v41, 1, v60
	v_lshl_add_u32 v42, v59, 1, v41
	v_cmp_lt_u32_e32 vcc, v41, v42
	s_and_saveexec_b64 s[58:59], vcc
	s_cbranch_execz .Lagg_taildone_0_0
	ds_read_u16 v40, v41
	v_add_u32_e32 v41, 2, v41
	s_waitcnt lgkmcnt(0)
	v_mad_u32_u16 v24, v40, s46, v1
	global_load_dwordx4 v[28:31], v24, s[48:49] offset:16
	global_load_dwordx4 v[24:27], v24, s[48:49]
.Lagg_loop_0_0:
	v_cmp_lt_u32_e32 vcc, v41, v42
	v_mov_b32_e32 v56, v43
	s_and_b64 s[60:61], exec, vcc
	s_cbranch_scc0 .Lagg_lastA_0_0
	s_mov_b64 s[62:63], exec
	s_mov_b64 exec, s[60:61]
	ds_read_u16 v40, v41
	v_add_u32_e32 v41, 2, v41
	s_waitcnt lgkmcnt(0)
	v_mad_u32_u16 v32, v40, s46, v1
	global_load_dwordx4 v[36:39], v32, s[48:49] offset:16
	global_load_dwordx4 v[32:35], v32, s[48:49]
	s_mov_b64 exec, s[62:63]
	s_waitcnt vmcnt(2)
	v_dot2c_f32_f16_e32 v56, v24, v16
	v_dot2c_f32_f16_e32 v56, v25, v17
	v_dot2c_f32_f16_e32 v56, v26, v18
	v_dot2c_f32_f16_e32 v56, v27, v19
	v_dot2c_f32_f16_e32 v56, v28, v20
	v_dot2c_f32_f16_e32 v56, v29, v21
	v_dot2c_f32_f16_e32 v56, v30, v22
	v_dot2c_f32_f16_e32 v56, v31, v23
	s_nop 2
	v_add_f32_dpp v56, v56, v56 quad_perm:[1,0,3,2] row_mask:0xf bank_mask:0xf bound_ctrl:1
	s_nop 0
	v_fmamk_f32 v58, v56, 0x3c23d70a, v44
	v_max_f32_e32 v56, v56, v58
	v_exp_f32_e32 v56, v56
	s_nop 0
	v_add_f32_e32 v45, v45, v56
	v_cvt_f16_f32_e32 v58, v56
	s_nop 0
	v_pk_fma_f16 v48, v24, v58, v48 op_sel_hi:[1,0,1]
	v_pk_fma_f16 v49, v25, v58, v49 op_sel_hi:[1,0,1]
	v_pk_fma_f16 v50, v26, v58, v50 op_sel_hi:[1,0,1]
	v_pk_fma_f16 v51, v27, v58, v51 op_sel_hi:[1,0,1]
	v_pk_fma_f16 v52, v28, v58, v52 op_sel_hi:[1,0,1]
	v_pk_fma_f16 v53, v29, v58, v53 op_sel_hi:[1,0,1]
	v_pk_fma_f16 v54, v30, v58, v54 op_sel_hi:[1,0,1]
	v_pk_fma_f16 v55, v31, v58, v55 op_sel_hi:[1,0,1]
	s_mov_b64 exec, s[60:61]
	v_cmp_lt_u32_e32 vcc, v41, v42
	v_mov_b32_e32 v56, v43
	s_and_b64 s[60:61], exec, vcc
	s_cbranch_scc0 .Lagg_lastB_0_0
	s_mov_b64 s[62:63], exec
	s_mov_b64 exec, s[60:61]
	ds_read_u16 v40, v41
	v_add_u32_e32 v41, 2, v41
	s_waitcnt lgkmcnt(0)
	v_mad_u32_u16 v24, v40, s46, v1
	global_load_dwordx4 v[28:31], v24, s[48:49] offset:16
	global_load_dwordx4 v[24:27], v24, s[48:49]
	s_mov_b64 exec, s[62:63]
	s_waitcnt vmcnt(2)
	v_dot2c_f32_f16_e32 v56, v32, v16
	v_dot2c_f32_f16_e32 v56, v33, v17
	v_dot2c_f32_f16_e32 v56, v34, v18
	v_dot2c_f32_f16_e32 v56, v35, v19
	v_dot2c_f32_f16_e32 v56, v36, v20
	v_dot2c_f32_f16_e32 v56, v37, v21
	v_dot2c_f32_f16_e32 v56, v38, v22
	v_dot2c_f32_f16_e32 v56, v39, v23
	s_nop 2
	v_add_f32_dpp v56, v56, v56 quad_perm:[1,0,3,2] row_mask:0xf bank_mask:0xf bound_ctrl:1
	s_nop 0
	v_fmamk_f32 v58, v56, 0x3c23d70a, v44
	v_max_f32_e32 v56, v56, v58
	v_exp_f32_e32 v56, v56
	s_nop 0
	v_add_f32_e32 v45, v45, v56
	v_cvt_f16_f32_e32 v58, v56
	s_nop 0
	v_pk_fma_f16 v48, v32, v58, v48 op_sel_hi:[1,0,1]
	v_pk_fma_f16 v49, v33, v58, v49 op_sel_hi:[1,0,1]
	v_pk_fma_f16 v50, v34, v58, v50 op_sel_hi:[1,0,1]
	v_pk_fma_f16 v51, v35, v58, v51 op_sel_hi:[1,0,1]
	v_pk_fma_f16 v52, v36, v58, v52 op_sel_hi:[1,0,1]
	v_pk_fma_f16 v53, v37, v58, v53 op_sel_hi:[1,0,1]
	v_pk_fma_f16 v54, v38, v58, v54 op_sel_hi:[1,0,1]
	v_pk_fma_f16 v55, v39, v58, v55 op_sel_hi:[1,0,1]
	s_mov_b64 exec, s[60:61]
	s_branch .Lagg_loop_0_0
.Lagg_lastA_0_0:
	s_waitcnt vmcnt(0)
	v_dot2c_f32_f16_e32 v56, v24, v16
	v_dot2c_f32_f16_e32 v56, v25, v17
	v_dot2c_f32_f16_e32 v56, v26, v18
	v_dot2c_f32_f16_e32 v56, v27, v19
	v_dot2c_f32_f16_e32 v56, v28, v20
	v_dot2c_f32_f16_e32 v56, v29, v21
	v_dot2c_f32_f16_e32 v56, v30, v22
	v_dot2c_f32_f16_e32 v56, v31, v23
	s_nop 2
	v_add_f32_dpp v56, v56, v56 quad_perm:[1,0,3,2] row_mask:0xf bank_mask:0xf bound_ctrl:1
	s_nop 0
	v_fmamk_f32 v58, v56, 0x3c23d70a, v44
	v_max_f32_e32 v56, v56, v58
	v_exp_f32_e32 v56, v56
	s_nop 0
	v_add_f32_e32 v45, v45, v56
	v_cvt_f16_f32_e32 v58, v56
	s_nop 0
	v_pk_fma_f16 v48, v24, v58, v48 op_sel_hi:[1,0,1]
	v_pk_fma_f16 v49, v25, v58, v49 op_sel_hi:[1,0,1]
	v_pk_fma_f16 v50, v26, v58, v50 op_sel_hi:[1,0,1]
	v_pk_fma_f16 v51, v27, v58, v51 op_sel_hi:[1,0,1]
	v_pk_fma_f16 v52, v28, v58, v52 op_sel_hi:[1,0,1]
	v_pk_fma_f16 v53, v29, v58, v53 op_sel_hi:[1,0,1]
	v_pk_fma_f16 v54, v30, v58, v54 op_sel_hi:[1,0,1]
	v_pk_fma_f16 v55, v31, v58, v55 op_sel_hi:[1,0,1]
	s_branch .Lagg_taildone_0_0
.Lagg_lastB_0_0:
	s_waitcnt vmcnt(0)
	v_dot2c_f32_f16_e32 v56, v32, v16
	v_dot2c_f32_f16_e32 v56, v33, v17
	v_dot2c_f32_f16_e32 v56, v34, v18
	v_dot2c_f32_f16_e32 v56, v35, v19
	v_dot2c_f32_f16_e32 v56, v36, v20
	v_dot2c_f32_f16_e32 v56, v37, v21
	v_dot2c_f32_f16_e32 v56, v38, v22
	v_dot2c_f32_f16_e32 v56, v39, v23
	s_nop 2
	v_add_f32_dpp v56, v56, v56 quad_perm:[1,0,3,2] row_mask:0xf bank_mask:0xf bound_ctrl:1
	s_nop 0
	v_fmamk_f32 v58, v56, 0x3c23d70a, v44
	v_max_f32_e32 v56, v56, v58
	v_exp_f32_e32 v56, v56
	s_nop 0
	v_add_f32_e32 v45, v45, v56
	v_cvt_f16_f32_e32 v58, v56
	s_nop 0
	v_pk_fma_f16 v48, v32, v58, v48 op_sel_hi:[1,0,1]
	v_pk_fma_f16 v49, v33, v58, v49 op_sel_hi:[1,0,1]
	v_pk_fma_f16 v50, v34, v58, v50 op_sel_hi:[1,0,1]
	v_pk_fma_f16 v51, v35, v58, v51 op_sel_hi:[1,0,1]
	v_pk_fma_f16 v52, v36, v58, v52 op_sel_hi:[1,0,1]
	v_pk_fma_f16 v53, v37, v58, v53 op_sel_hi:[1,0,1]
	v_pk_fma_f16 v54, v38, v58, v54 op_sel_hi:[1,0,1]
	v_pk_fma_f16 v55, v39, v58, v55 op_sel_hi:[1,0,1]
.Lagg_taildone_0_0:
	s_mov_b64 exec, s[58:59]
	v_lshlrev_b32_e32 v61, 2, v2
	ds_read_b32 v59, v61 offset:33552
	ds_read_b32 v60, v61 offset:37648
	s_waitcnt lgkmcnt(0)
	v_lshlrev_b32_e32 v41, 1, v60
	v_lshl_add_u32 v42, v59, 1, v41
	v_cmp_lt_u32_e32 vcc, v41, v42
	s_and_saveexec_b64 s[58:59], vcc
	s_cbranch_execz .Lagg_taildone_0_1
	ds_read_u16 v40, v41
	v_add_u32_e32 v41, 2, v41
	s_waitcnt lgkmcnt(0)
	v_mad_u32_u16 v24, v40, s46, v1
	global_load_dwordx4 v[28:31], v24, s[48:49] offset:16
	global_load_dwordx4 v[24:27], v24, s[48:49]

.Lagg_taildone_0_1:
	s_mov_b64 exec, s[58:59]
	v_sub_f32_e32 v58, v14, v46
	v_exp_f32_e32 v58, v58
	v_mul_f32_e32 v59, 0x33000000, v45
	v_rcp_f32_e32 v47, v45
	v_mul_f32_e32 v58, 0x24e69595, v58
	v_fma_f32 v60, -v45, v47, 1.0
	v_cmp_ge_f32_e64 s[62:63], v59, v58
	v_cmp_eq_f32_e32 vcc, 0, v45
	v_fmac_f32_e32 v47, v60, v47
	s_nop 1
	v_cndmask_b32_e64 v47, v47, 0, vcc
	s_or_b64 s[62:63], s[62:63], vcc
	s_mov_b64 s[66:67], exec
	s_andn2_b64 exec, exec, s[62:63]
	s_cbranch_execnz .Lagg_gmax_0
.Lagg_gmaxret_0:
	s_mov_b64 exec, s[66:67]
.Lagg_fin_0:
	v_fma_mix_f32 v32, v48, v47, 0 op_sel_hi:[1,0,0]
	v_fma_mix_f32 v33, v48, v47, 0 op_sel:[1,0,0] op_sel_hi:[1,0,0]
	v_fma_mix_f32 v34, v49, v47, 0 op_sel_hi:[1,0,0]
	v_fma_mix_f32 v35, v49, v47, 0 op_sel:[1,0,0] op_sel_hi:[1,0,0]
	v_fma_mix_f32 v36, v50, v47, 0 op_sel_hi:[1,0,0]
	v_fma_mix_f32 v37, v50, v47, 0 op_sel:[1,0,0] op_sel_hi:[1,0,0]
	v_fma_mix_f32 v38, v51, v47, 0 op_sel_hi:[1,0,0]
	v_fma_mix_f32 v39, v51, v47, 0 op_sel:[1,0,0] op_sel_hi:[1,0,0]
	v_fma_mix_f32 v56, v52, v47, 0 op_sel_hi:[1,0,0]
	v_fma_mix_f32 v57, v52, v47, 0 op_sel:[1,0,0] op_sel_hi:[1,0,0]
	v_fma_mix_f32 v58, v53, v47, 0 op_sel_hi:[1,0,0]
	v_fma_mix_f32 v59, v53, v47, 0 op_sel:[1,0,0] op_sel_hi:[1,0,0]
	v_fma_mix_f32 v60, v54, v47, 0 op_sel_hi:[1,0,0]
	v_fma_mix_f32 v61, v54, v47, 0 op_sel:[1,0,0] op_sel_hi:[1,0,0]
	v_fma_mix_f32 v62, v55, v47, 0 op_sel_hi:[1,0,0]
	v_fma_mix_f32 v63, v55, v47, 0 op_sel:[1,0,0] op_sel_hi:[1,0,0]
	v_cvt_pk_f16_f32 v5, v32, v33
	v_cvt_pk_f16_f32 v6, v34, v35
	v_cvt_pk_f16_f32 v7, v36, v37
	v_cvt_pk_f16_f32 v8, v38, v39
	v_cvt_pk_f16_f32 v9, v56, v57
	v_cvt_pk_f16_f32 v10, v58, v59
	v_cvt_pk_f16_f32 v11, v60, v61
	v_cvt_pk_f16_f32 v12, v62, v63
	s_mul_i32 s52, s3, 0x61a800
	s_add_u32 s52, s52, 0xc35000
	s_add_u32 s48, s12, s52
	s_addc_u32 s49, s13, 0
	s_lshl_b32 s52, s3, 7
	s_add_u32 s52, s52, 0x100
	s_add_u32 s52, s18, s52
	s_addc_u32 s53, s19, 0
	global_load_dwordx4 v[16:19], v1, s[52:53]
	global_load_dwordx4 v[20:23], v1, s[52:53] offset:16
	global_load_dword v56, v13, s[20:21] offset:32
	global_load_dword v57, v13, s[20:21] offset:48
	s_waitcnt vmcnt(0)
	v_not_b32_e32 v58, v56
	v_and_b32_e32 v59, 0x7fffffff, v56
	v_cmp_gt_i32_e32 vcc, 0, v56
	s_nop 1
	v_cndmask_b32_e32 v56, v58, v59, vcc
	v_not_b32_e32 v58, v57
	v_and_b32_e32 v59, 0x7fffffff, v57
	v_cmp_gt_i32_e32 vcc, 0, v57
	s_nop 1
	v_cndmask_b32_e32 v57, v58, v59, vcc
	v_add_f32_e32 v14, v56, v57
	v_mul_f32_e32 v58, 0x3c23d70a, v14
	v_max_f32_e32 v14, v14, v58
	v_add_f32_e32 v46, v56, v4
	v_mul_f32_e32 v58, 0x3c23d70a, v46
	v_max_f32_e32 v46, v46, v58
	v_sub_f32_e32 v43, v4, v46
	v_mul_f32_e32 v43, 0.5, v43
	v_mul_f32_e32 v44, 0xbf7d70a4, v46
	v_mov_b32_e32 v45, 0
	v_mov_b32_e32 v48, 0
	v_mov_b32_e32 v49, 0
	v_mov_b32_e32 v50, 0
	v_mov_b32_e32 v51, 0
	v_mov_b32_e32 v52, 0
	v_mov_b32_e32 v53, 0
	v_mov_b32_e32 v54, 0
	v_mov_b32_e32 v55, 0
	s_cmp_eq_u32 s7, 0
	s_cbranch_scc1 .Lagg_slow_1
	v_lshlrev_b32_e32 v61, 2, v2
	ds_read_b32 v59, v61 offset:34816
	ds_read_b32 v60, v61 offset:38912
	s_waitcnt lgkmcnt(0)
	v_lshlrev_b32_e32 v41, 1, v60
	v_add_u32_e32 v41, 0x4000, v41
	v_lshl_add_u32 v42, v59, 1, v41
	v_cmp_lt_u32_e32 vcc, v41, v42
	s_and_saveexec_b64 s[58:59], vcc
	s_cbranch_execz .Lagg_taildone_1_0
	ds_read_u16 v40, v41
	v_add_u32_e32 v41, 2, v41
	s_waitcnt lgkmcnt(0)
	v_mad_u32_u16 v24, v40, s46, v1
	global_load_dwordx4 v[28:31], v24, s[48:49] offset:16
	global_load_dwordx4 v[24:27], v24, s[48:49]

.Lagg_taildone_1_0:
	s_mov_b64 exec, s[58:59]
	v_lshlrev_b32_e32 v61, 2, v2
	ds_read_b32 v59, v61 offset:35600
	ds_read_b32 v60, v61 offset:39696
	s_waitcnt lgkmcnt(0)
	v_lshlrev_b32_e32 v41, 1, v60
	v_add_u32_e32 v41, 0x4000, v41
	v_lshl_add_u32 v42, v59, 1, v41
	v_cmp_lt_u32_e32 vcc, v41, v42
	s_and_saveexec_b64 s[58:59], vcc
	s_cbranch_execz .Lagg_taildone_1_1
	ds_read_u16 v40, v41
	v_add_u32_e32 v41, 2, v41
	s_waitcnt lgkmcnt(0)
	v_mad_u32_u16 v24, v40, s46, v1
	global_load_dwordx4 v[28:31], v24, s[48:49] offset:16
	global_load_dwordx4 v[24:27], v24, s[48:49]

.Lagg_taildone_1_1:
	s_mov_b64 exec, s[58:59]
	v_add_u32_e32 v61, s6, v2
	v_mad_u32_u24 v40, v61, s46, v1
	global_load_dwordx4 v[24:27], v40, s[70:71] nt
	global_load_dwordx4 v[28:31], v40, s[70:71] offset:16 nt
	v_lshlrev_b32_e32 v41, 9, v61
	v_lshl_add_u32 v41, v1, 1, v41
	v_sub_f32_e32 v58, v14, v46
	v_exp_f32_e32 v58, v58
	v_mul_f32_e32 v59, 0x33000000, v45
	v_rcp_f32_e32 v47, v45
	v_mul_f32_e32 v58, 0x24e69595, v58
	v_fma_f32 v60, -v45, v47, 1.0
	v_cmp_ge_f32_e64 s[62:63], v59, v58
	v_cmp_eq_f32_e32 vcc, 0, v45
	v_fmac_f32_e32 v47, v60, v47
	s_nop 1
	v_cndmask_b32_e64 v47, v47, 0, vcc
	s_or_b64 s[62:63], s[62:63], vcc
	s_mov_b64 s[66:67], exec
	s_andn2_b64 exec, exec, s[62:63]
	s_cbranch_execnz .Lagg_gmax_1

.Lagg_fin_1:
	v_fma_mix_f32 v32, v48, v47, 0 op_sel_hi:[1,0,0]
	v_fma_mix_f32 v33, v48, v47, 0 op_sel:[1,0,0] op_sel_hi:[1,0,0]
	v_fma_mix_f32 v34, v49, v47, 0 op_sel_hi:[1,0,0]
	v_fma_mix_f32 v35, v49, v47, 0 op_sel:[1,0,0] op_sel_hi:[1,0,0]
	v_fma_mix_f32 v36, v50, v47, 0 op_sel_hi:[1,0,0]
	v_fma_mix_f32 v37, v50, v47, 0 op_sel:[1,0,0] op_sel_hi:[1,0,0]
	v_fma_mix_f32 v38, v51, v47, 0 op_sel_hi:[1,0,0]
	v_fma_mix_f32 v39, v51, v47, 0 op_sel:[1,0,0] op_sel_hi:[1,0,0]
	v_fma_mix_f32 v56, v52, v47, 0 op_sel_hi:[1,0,0]
	v_fma_mix_f32 v57, v52, v47, 0 op_sel:[1,0,0] op_sel_hi:[1,0,0]
	v_fma_mix_f32 v58, v53, v47, 0 op_sel_hi:[1,0,0]
	v_fma_mix_f32 v59, v53, v47, 0 op_sel:[1,0,0] op_sel_hi:[1,0,0]
	v_fma_mix_f32 v60, v54, v47, 0 op_sel_hi:[1,0,0]
	v_fma_mix_f32 v61, v54, v47, 0 op_sel:[1,0,0] op_sel_hi:[1,0,0]
	v_fma_mix_f32 v62, v55, v47, 0 op_sel_hi:[1,0,0]
	v_fma_mix_f32 v63, v55, v47, 0 op_sel:[1,0,0] op_sel_hi:[1,0,0]
	v_fma_mix_f32 v32, v5, v15, v32 op_sel_hi:[1,0,0]
	v_fma_mix_f32 v33, v5, v15, v33 op_sel:[1,0,0] op_sel_hi:[1,0,0]
	v_fma_mix_f32 v34, v6, v15, v34 op_sel_hi:[1,0,0]
	v_fma_mix_f32 v35, v6, v15, v35 op_sel:[1,0,0] op_sel_hi:[1,0,0]
	v_fma_mix_f32 v36, v7, v15, v36 op_sel_hi:[1,0,0]
	v_fma_mix_f32 v37, v7, v15, v37 op_sel:[1,0,0] op_sel_hi:[1,0,0]
	v_fma_mix_f32 v38, v8, v15, v38 op_sel_hi:[1,0,0]
	v_fma_mix_f32 v39, v8, v15, v39 op_sel:[1,0,0] op_sel_hi:[1,0,0]
	v_fma_mix_f32 v56, v9, v15, v56 op_sel_hi:[1,0,0]
	v_fma_mix_f32 v57, v9, v15, v57 op_sel:[1,0,0] op_sel_hi:[1,0,0]
	v_fma_mix_f32 v58, v10, v15, v58 op_sel_hi:[1,0,0]
	v_fma_mix_f32 v59, v10, v15, v59 op_sel:[1,0,0] op_sel_hi:[1,0,0]
	v_fma_mix_f32 v60, v11, v15, v60 op_sel_hi:[1,0,0]
	v_fma_mix_f32 v61, v11, v15, v61 op_sel:[1,0,0] op_sel_hi:[1,0,0]
	v_fma_mix_f32 v62, v12, v15, v62 op_sel_hi:[1,0,0]
	v_fma_mix_f32 v63, v12, v15, v63 op_sel:[1,0,0] op_sel_hi:[1,0,0]
	s_waitcnt vmcnt(0)
	v_fma_mix_f32 v32, v24, v15, v32 op_sel_hi:[1,0,0]
	v_fma_mix_f32 v33, v24, v15, v33 op_sel:[1,0,0] op_sel_hi:[1,0,0]
	v_fma_mix_f32 v34, v25, v15, v34 op_sel_hi:[1,0,0]
	v_fma_mix_f32 v35, v25, v15, v35 op_sel:[1,0,0] op_sel_hi:[1,0,0]
	v_fma_mix_f32 v36, v26, v15, v36 op_sel_hi:[1,0,0]
	v_fma_mix_f32 v37, v26, v15, v37 op_sel:[1,0,0] op_sel_hi:[1,0,0]
	v_fma_mix_f32 v38, v27, v15, v38 op_sel_hi:[1,0,0]
	v_fma_mix_f32 v39, v27, v15, v39 op_sel:[1,0,0] op_sel_hi:[1,0,0]
	v_fma_mix_f32 v56, v28, v15, v56 op_sel_hi:[1,0,0]
	v_fma_mix_f32 v57, v28, v15, v57 op_sel:[1,0,0] op_sel_hi:[1,0,0]
	v_fma_mix_f32 v58, v29, v15, v58 op_sel_hi:[1,0,0]
	v_fma_mix_f32 v59, v29, v15, v59 op_sel:[1,0,0] op_sel_hi:[1,0,0]
	v_fma_mix_f32 v60, v30, v15, v60 op_sel_hi:[1,0,0]
	v_fma_mix_f32 v61, v30, v15, v61 op_sel:[1,0,0] op_sel_hi:[1,0,0]
	v_fma_mix_f32 v62, v31, v15, v62 op_sel_hi:[1,0,0]
	v_fma_mix_f32 v63, v31, v15, v63 op_sel:[1,0,0] op_sel_hi:[1,0,0]
	v_max_f32_e32 v32, 0, v32
	v_max_f32_e32 v33, 0, v33
	v_max_f32_e32 v34, 0, v34
	v_max_f32_e32 v35, 0, v35
	v_max_f32_e32 v36, 0, v36
	v_max_f32_e32 v37, 0, v37
	v_max_f32_e32 v38, 0, v38
	v_max_f32_e32 v39, 0, v39
	v_max_f32_e32 v56, 0, v56
	v_max_f32_e32 v57, 0, v57
	v_max_f32_e32 v58, 0, v58
	v_max_f32_e32 v59, 0, v59
	v_max_f32_e32 v60, 0, v60
	v_max_f32_e32 v61, 0, v61
	v_max_f32_e32 v62, 0, v62
	v_max_f32_e32 v63, 0, v63
	global_store_dwordx4 v41, v[32:35], s[68:69] nt
	global_store_dwordx4 v41, v[36:39], s[68:69] offset:16 nt
	global_store_dwordx4 v41, v[56:59], s[68:69] offset:32 nt
	global_store_dwordx4 v41, v[60:63], s[68:69] offset:48 nt
	s_nop 1

.Lagg_gmax_0:
	v_add_u32_e32 v58, 0, v13
	v_lshrrev_b32_e32 v59, 3, v1
	v_and_b32_e32 v59, 4, v59
	v_mov_b32_e32 v62, 0xff800000
	s_mov_b32 s52, 0
.Lagg_gmaxloop_0:
	global_load_dword v60, v59, s[24:25]
	global_load_dword v61, v59, s[22:23]
	s_waitcnt vmcnt(0)
	v_lshl_add_u32 v60, v60, 6, v58
	v_lshl_add_u32 v61, v61, 6, v58
	global_load_dword v60, v60, s[16:17]
	global_load_dword v61, v61, s[16:17] offset:16
	v_add_u32_e32 v59, 8, v59
	s_add_u32 s52, s52, 2
	s_cmp_lt_u32 s52, 0xc3500
	s_waitcnt vmcnt(0)
	v_add_f32_e32 v60, v60, v61
	v_max_f32_e32 v62, v62, v60
	s_cbranch_scc1 .Lagg_gmaxloop_0
	s_nop 1
	v_mov_b32_dpp v60, v62 quad_perm:[1,0,3,2] row_mask:0xf bank_mask:0xf bound_ctrl:1
	s_nop 0
	v_max_f32_e32 v62, v62, v60
	v_mul_f32_e32 v60, 0x3c23d70a, v62
	v_max_f32_e32 v62, v62, v60
	v_sub_f32_e32 v62, v62, v46
	v_exp_f32_e32 v62, v62
	v_mov_b32_e32 v60, v45
	v_fmac_f32_e32 v60, 0x24e69595, v62
	s_nop 0
	v_rcp_f32_e32 v47, v60
	s_nop 0
	v_fma_f32 v62, -v60, v47, 1.0
	v_fmac_f32_e32 v47, v62, v47
	s_branch .Lagg_gmaxret_0
.Lagg_slow_0:
	s_mov_b64 s[58:59], exec
	s_mov_b32 s52, 0
	s_mov_b32 s53, 0
	s_cmp_lt_u32 s52, s38
	s_cbranch_scc0 .Lagg_slowdone_0
.Lagg_slowloop_0:
	s_load_dword s54, s[42:43], s53
	s_waitcnt lgkmcnt(0)
	s_bfe_u32 s64, s54, 0x70010
	s_bfe_u32 s65, s54, 0x10017
	s_mul_i32 s65, s65, 0x62
	s_add_u32 s64, s64, s65
	s_and_b32 s54, s54, 0xffff
	s_mul_i32 s54, s54, s46
	v_cmp_eq_u32_e32 vcc, s64, v2
	s_and_saveexec_b64 s[62:63], vcc
	s_cbranch_execz .Lagg_slownext_0
	v_add_u32_e32 v24, s54, v1
	global_load_dwordx4 v[28:31], v24, s[48:49] offset:16
	global_load_dwordx4 v[24:27], v24, s[48:49]
	v_mov_b32_e32 v56, v43
	s_waitcnt vmcnt(0)
	v_dot2c_f32_f16_e32 v56, v24, v16
	v_dot2c_f32_f16_e32 v56, v25, v17
	v_dot2c_f32_f16_e32 v56, v26, v18
	v_dot2c_f32_f16_e32 v56, v27, v19
	v_dot2c_f32_f16_e32 v56, v28, v20
	v_dot2c_f32_f16_e32 v56, v29, v21
	v_dot2c_f32_f16_e32 v56, v30, v22
	v_dot2c_f32_f16_e32 v56, v31, v23
	s_nop 2
	v_add_f32_dpp v56, v56, v56 quad_perm:[1,0,3,2] row_mask:0xf bank_mask:0xf bound_ctrl:1
	s_nop 0
	v_fmamk_f32 v58, v56, 0x3c23d70a, v44
	v_max_f32_e32 v56, v56, v58
	v_exp_f32_e32 v56, v56
	s_nop 0
	v_add_f32_e32 v45, v45, v56
	v_cvt_f16_f32_e32 v58, v56
	s_nop 0
	v_pk_fma_f16 v48, v24, v58, v48 op_sel_hi:[1,0,1]
	v_pk_fma_f16 v49, v25, v58, v49 op_sel_hi:[1,0,1]
	v_pk_fma_f16 v50, v26, v58, v50 op_sel_hi:[1,0,1]
	v_pk_fma_f16 v51, v27, v58, v51 op_sel_hi:[1,0,1]
	v_pk_fma_f16 v52, v28, v58, v52 op_sel_hi:[1,0,1]
	v_pk_fma_f16 v53, v29, v58, v53 op_sel_hi:[1,0,1]
	v_pk_fma_f16 v54, v30, v58, v54 op_sel_hi:[1,0,1]
	v_pk_fma_f16 v55, v31, v58, v55 op_sel_hi:[1,0,1]
.Lagg_slownext_0:
	s_mov_b64 exec, s[62:63]
	s_add_u32 s52, s52, 1
	s_add_u32 s53, s53, 4
	s_cmp_lt_u32 s52, s38
	s_cbranch_scc1 .Lagg_slowloop_0
.Lagg_slowdone_0:
	s_branch .Lagg_taildone_0_1
.Lagg_gmax_1:
	v_add_u32_e32 v58, 32, v13
	v_lshrrev_b32_e32 v59, 3, v1
	v_and_b32_e32 v59, 4, v59
	v_mov_b32_e32 v62, 0xff800000
	s_mov_b32 s52, 0
.Lagg_gmaxloop_1:
	global_load_dword v60, v59, s[28:29]
	global_load_dword v61, v59, s[26:27]
	s_waitcnt vmcnt(0)
	v_lshl_add_u32 v60, v60, 6, v58
	v_lshl_add_u32 v61, v61, 6, v58
	global_load_dword v60, v60, s[16:17]
	global_load_dword v61, v61, s[16:17] offset:16
	v_add_u32_e32 v59, 8, v59
	s_add_u32 s52, s52, 2
	s_cmp_lt_u32 s52, 0xc3500
	s_waitcnt vmcnt(0)
	v_add_f32_e32 v60, v60, v61
	v_max_f32_e32 v62, v62, v60
	s_cbranch_scc1 .Lagg_gmaxloop_1
	s_nop 1
	v_mov_b32_dpp v60, v62 quad_perm:[1,0,3,2] row_mask:0xf bank_mask:0xf bound_ctrl:1
	s_nop 0
	v_max_f32_e32 v62, v62, v60
	v_mul_f32_e32 v60, 0x3c23d70a, v62
	v_max_f32_e32 v62, v62, v60
	v_sub_f32_e32 v62, v62, v46
	v_exp_f32_e32 v62, v62
	v_mov_b32_e32 v60, v45
	v_fmac_f32_e32 v60, 0x24e69595, v62
	s_nop 0
	v_rcp_f32_e32 v47, v60
	s_nop 0
	v_fma_f32 v62, -v60, v47, 1.0
	v_fmac_f32_e32 v47, v62, v47
	s_branch .Lagg_gmaxret_1
.Lagg_slow_1:
	s_mov_b64 s[58:59], exec
	s_mov_b32 s52, 0
	s_mov_b32 s53, 0
	s_cmp_lt_u32 s52, s39
	s_cbranch_scc0 .Lagg_slowdone_1
.Lagg_slowloop_1:
	s_load_dword s54, s[44:45], s53
	s_waitcnt lgkmcnt(0)
	s_bfe_u32 s64, s54, 0x70010
	s_bfe_u32 s65, s54, 0x10017
	s_mul_i32 s65, s65, 0x62
	s_add_u32 s64, s64, s65
	s_and_b32 s54, s54, 0xffff
	s_mul_i32 s54, s54, s46
	v_cmp_eq_u32_e32 vcc, s64, v2
	s_and_saveexec_b64 s[62:63], vcc
	s_cbranch_execz .Lagg_slownext_1
	v_add_u32_e32 v24, s54, v1
	global_load_dwordx4 v[28:31], v24, s[48:49] offset:16
	global_load_dwordx4 v[24:27], v24, s[48:49]
	v_mov_b32_e32 v56, v43
	s_waitcnt vmcnt(0)
	v_dot2c_f32_f16_e32 v56, v24, v16
	v_dot2c_f32_f16_e32 v56, v25, v17
	v_dot2c_f32_f16_e32 v56, v26, v18
	v_dot2c_f32_f16_e32 v56, v27, v19
	v_dot2c_f32_f16_e32 v56, v28, v20
	v_dot2c_f32_f16_e32 v56, v29, v21
	v_dot2c_f32_f16_e32 v56, v30, v22
	v_dot2c_f32_f16_e32 v56, v31, v23
	s_nop 2
	v_add_f32_dpp v56, v56, v56 quad_perm:[1,0,3,2] row_mask:0xf bank_mask:0xf bound_ctrl:1
	s_nop 0
	v_fmamk_f32 v58, v56, 0x3c23d70a, v44
	v_max_f32_e32 v56, v56, v58
	v_exp_f32_e32 v56, v56
	s_nop 0
	v_add_f32_e32 v45, v45, v56
	v_cvt_f16_f32_e32 v58, v56
	s_nop 0
	v_pk_fma_f16 v48, v24, v58, v48 op_sel_hi:[1,0,1]
	v_pk_fma_f16 v49, v25, v58, v49 op_sel_hi:[1,0,1]
	v_pk_fma_f16 v50, v26, v58, v50 op_sel_hi:[1,0,1]
	v_pk_fma_f16 v51, v27, v58, v51 op_sel_hi:[1,0,1]
	v_pk_fma_f16 v52, v28, v58, v52 op_sel_hi:[1,0,1]
	v_pk_fma_f16 v53, v29, v58, v53 op_sel_hi:[1,0,1]
	v_pk_fma_f16 v54, v30, v58, v54 op_sel_hi:[1,0,1]
	v_pk_fma_f16 v55, v31, v58, v55 op_sel_hi:[1,0,1]
.Lagg_slownext_1:
	s_mov_b64 exec, s[62:63]
	s_add_u32 s52, s52, 1
	s_add_u32 s53, s53, 4
	s_cmp_lt_u32 s52, s39
	s_cbranch_scc1 .Lagg_slowloop_1

	.amdhsa_kernel _Z10agg_kernelPKjPKiPKDF16_S4_PKfS4_S0_S2_S2_S2_S2_Pf
		.amdhsa_group_segment_fixed_size 41216
		.amdhsa_private_segment_fixed_size 0
		.amdhsa_kernarg_size 96
		.amdhsa_user_sgpr_count 2
		.amdhsa_user_sgpr_dispatch_ptr 0
		.amdhsa_user_sgpr_queue_ptr 0
		.amdhsa_user_sgpr_kernarg_segment_ptr 1
		.amdhsa_user_sgpr_dispatch_id 0
		.amdhsa_user_sgpr_kernarg_preload_length 0
		.amdhsa_user_sgpr_kernarg_preload_offset 0
		.amdhsa_user_sgpr_private_segment_size 0
		.amdhsa_uses_dynamic_stack 0
		.amdhsa_enable_private_segment 0
		.amdhsa_system_sgpr_workgroup_id_x 1
		.amdhsa_system_sgpr_workgroup_id_y 0
		.amdhsa_system_sgpr_workgroup_id_z 0
		.amdhsa_system_sgpr_workgroup_info 0
		.amdhsa_system_vgpr_workitem_id 0
		.amdhsa_next_free_vgpr 64
		.amdhsa_next_free_sgpr 72
		.amdhsa_accum_offset 64
		.amdhsa_reserve_vcc 1
		.amdhsa_float_round_mode_32 0
		.amdhsa_float_round_mode_16_64 0
		.amdhsa_float_denorm_mode_32 3
		.amdhsa_float_denorm_mode_16_64 3
		.amdhsa_dx10_clamp 1
		.amdhsa_ieee_mode 1
		.amdhsa_fp16_overflow 0
		.amdhsa_tg_split 0
		.amdhsa_exception_fp_ieee_invalid_op 0
		.amdhsa_exception_fp_denorm_src 0
		.amdhsa_exception_fp_ieee_div_zero 0
		.amdhsa_exception_fp_ieee_overflow 0
		.amdhsa_exception_fp_ieee_underflow 0
		.amdhsa_exception_fp_ieee_inexact 0
		.amdhsa_exception_int_div_zero 0
	.end_amdhsa_kernel

amdhsa.kernels:
  - .agpr_count:     0
    .args:
      - .actual_access:  read_only
        .address_space:  global
        .offset:         0
        .size:           8
        .value_kind:     global_buffer
      - .actual_access:  read_only
        .address_space:  global
        .offset:         8
        .size:           8
        .value_kind:     global_buffer
      - .actual_access:  read_only
        .address_space:  global
        .offset:         16
        .size:           8
        .value_kind:     global_buffer
      - .actual_access:  read_only
        .address_space:  global
        .offset:         24
        .size:           8
        .value_kind:     global_buffer
      - .actual_access:  read_only
        .address_space:  global
        .offset:         32
        .size:           8
        .value_kind:     global_buffer
      - .actual_access:  read_only
        .address_space:  global
        .offset:         40
        .size:           8
        .value_kind:     global_buffer
      - .actual_access:  read_only
        .address_space:  global
        .offset:         48
        .size:           8
        .value_kind:     global_buffer
      - .actual_access:  write_only
        .address_space:  global
        .offset:         56
        .size:           8
        .value_kind:     global_buffer
      - .actual_access:  write_only
        .address_space:  global
        .offset:         64
        .size:           8
        .value_kind:     global_buffer
      - .actual_access:  write_only
        .address_space:  global
        .offset:         72
        .size:           8
        .value_kind:     global_buffer
      - .actual_access:  write_only
        .address_space:  global
        .offset:         80
        .size:           8
        .value_kind:     global_buffer
      - .actual_access:  read_only
        .address_space:  global
        .offset:         88
        .size:           8
        .value_kind:     global_buffer
      - .actual_access:  read_only
        .address_space:  global
        .offset:         96
        .size:           8
        .value_kind:     global_buffer
      - .actual_access:  write_only
        .address_space:  global
        .offset:         104
        .size:           8
        .value_kind:     global_buffer
    .group_segment_fixed_size: 1024
    .kernarg_segment_align: 8
    .kernarg_segment_size: 112
    .language:       OpenCL C
    .language_version:
      - 2
      - 0
    .max_flat_workgroup_size: 1024
    .name:           _Z17prep_count_kernelPKfS0_S0_S0_S0_S0_S0_PDF16_PjPfS1_PKiS5_Pi
    .private_segment_fixed_size: 0
    .sgpr_count:     27
    .sgpr_spill_count: 0
    .symbol:         _Z17prep_count_kernelPKfS0_S0_S0_S0_S0_S0_PDF16_PjPfS1_PKiS5_Pi.kd
    .uniform_work_group_size: 1
    .uses_dynamic_stack: false
    .vgpr_count:     62
    .vgpr_spill_count: 0
    .wavefront_size: 64
  - .agpr_count:     0
    .args:
      - .actual_access:  read_only
        .address_space:  global
        .offset:         0
        .size:           8
        .value_kind:     global_buffer
      - .actual_access:  read_only
        .address_space:  global
        .offset:         8
        .size:           8
        .value_kind:     global_buffer
      - .actual_access:  read_only
        .address_space:  global
        .offset:         16
        .size:           8
        .value_kind:     global_buffer
      - .actual_access:  write_only
        .address_space:  global
        .offset:         24
        .size:           8
        .value_kind:     global_buffer
      - .actual_access:  write_only
        .address_space:  global
        .offset:         32
        .size:           8
        .value_kind:     global_buffer
      - .actual_access:  write_only
        .address_space:  global
        .offset:         40
        .size:           8
        .value_kind:     global_buffer
      - .address_space:  global
        .offset:         48
        .size:           8
        .value_kind:     global_buffer
      - .actual_access:  read_only
        .address_space:  global
        .offset:         56
        .size:           8
        .value_kind:     global_buffer
      - .actual_access:  read_only
        .address_space:  global
        .offset:         64
        .size:           8
        .value_kind:     global_buffer
      - .actual_access:  read_only
        .address_space:  global
        .offset:         72
        .size:           8
        .value_kind:     global_buffer
      - .actual_access:  read_only
        .address_space:  global
        .offset:         80
        .size:           8
        .value_kind:     global_buffer
      - .actual_access:  read_only
        .address_space:  global
        .offset:         88
        .size:           8
        .value_kind:     global_buffer
      - .actual_access:  write_only
        .address_space:  global
        .offset:         96
        .size:           8
        .value_kind:     global_buffer
      - .actual_access:  write_only
        .address_space:  global
        .offset:         104
        .size:           8
        .value_kind:     global_buffer
    .group_segment_fixed_size: 144320
    .kernarg_segment_align: 8
    .kernarg_segment_size: 112
    .language:       OpenCL C
    .language_version:
      - 2
      - 0
    .max_flat_workgroup_size: 512
    .name:           _Z19gemm_scatter_kernelPKfPKDF16_S0_PDF16_S3_PfPjPKiS7_S7_S7_S7_PiS5_
    .private_segment_fixed_size: 0
    .sgpr_count:     46
    .sgpr_spill_count: 0
    .symbol:         _Z19gemm_scatter_kernelPKfPKDF16_S0_PDF16_S3_PfPjPKiS7_S7_S7_S7_PiS5_.kd
    .uniform_work_group_size: 1
    .uses_dynamic_stack: false
    .vgpr_count:     230
    .vgpr_spill_count: 0
    .wavefront_size: 64
  - .agpr_count:     0
    .args:
      - .actual_access:  read_only
        .address_space:  global
        .offset:         0
        .size:           8
        .value_kind:     global_buffer
      - .actual_access:  read_only
        .address_space:  global
        .offset:         8
        .size:           8
        .value_kind:     global_buffer
      - .actual_access:  read_only
        .address_space:  global
        .offset:         16
        .size:           8
        .value_kind:     global_buffer
      - .actual_access:  read_only
        .address_space:  global
        .offset:         24
        .size:           8
        .value_kind:     global_buffer
      - .actual_access:  read_only
        .address_space:  global
        .offset:         32
        .size:           8
        .value_kind:     global_buffer
      - .actual_access:  read_only
        .address_space:  global
        .offset:         40
        .size:           8
        .value_kind:     global_buffer
      - .actual_access:  read_only
        .address_space:  global
        .offset:         48
        .size:           8
        .value_kind:     global_buffer
      - .actual_access:  read_only
        .address_space:  global
        .offset:         56
        .size:           8
        .value_kind:     global_buffer
      - .actual_access:  read_only
        .address_space:  global
        .offset:         64
        .size:           8
        .value_kind:     global_buffer
      - .actual_access:  read_only
        .address_space:  global
        .offset:         72
        .size:           8
        .value_kind:     global_buffer
      - .actual_access:  read_only
        .address_space:  global
        .offset:         80
        .size:           8
        .value_kind:     global_buffer
      - .actual_access:  write_only
        .address_space:  global
        .offset:         88
        .size:           8
        .value_kind:     global_buffer
    .group_segment_fixed_size: 41216
    .kernarg_segment_align: 8
    .kernarg_segment_size: 96
    .language:       OpenCL C
    .language_version:
      - 2
      - 0
    .max_flat_workgroup_size: 1024
    .name:           _Z10agg_kernelPKjPKiPKDF16_S4_PKfS4_S0_S2_S2_S2_S2_Pf
    .private_segment_fixed_size: 0
    .sgpr_count:     78
    .sgpr_spill_count: 0
    .symbol:         _Z10agg_kernelPKjPKiPKDF16_S4_PKfS4_S0_S2_S2_S2_S2_Pf.kd
    .uniform_work_group_size: 1
    .uses_dynamic_stack: false
    .vgpr_count:     64
    .vgpr_spill_count: 0
    .wavefront_size: 64
